# stack4 + packed f32 ops beside MFMAs split into scalar ops in the GLA scan step and the NAT attention tiles (strategy 7)
# speedup vs baseline: 1.0015x; 1.0015x over previous
.LBB0_1593:
	s_add_i32 s6, s24, s28
	s_cmp_gt_u32 s28, 22
	s_cselect_b64 s[0:1], -1, 0
	s_cmp_ge_i32 s6, s22
	s_cselect_b64 s[14:15], -1, 0
	s_add_i32 s26, s22, 8
	s_cmp_lt_i32 s6, s26
	s_cselect_b64 s[16:17], -1, 0
	s_and_b64 s[14:15], s[14:15], s[16:17]
	s_or_b64 s[16:17], s[0:1], s[14:15]
	s_cmp_ge_i32 s6, s23
	s_cselect_b64 s[14:15], -1, 0
	s_add_i32 s27, s23, 8
	s_cmp_lt_i32 s6, s27
	s_cselect_b64 s[30:31], -1, 0
	s_and_b64 s[14:15], s[14:15], s[30:31]
	s_or_b64 s[30:31], s[16:17], s[14:15]
	s_andn2_b64 vcc, exec, s[30:31]
	s_cbranch_vccnz .LBB0_1610
	v_add_u32_e32 v4, v225, v226
	ds_read_b128 v[154:157], v224
	ds_read_b128 v[158:161], v224 offset:64
	ds_read_b128 v[174:177], v224 offset:4608
	ds_read_b128 v[162:165], v224 offset:4672
	ds_read_b128 v[166:169], v224 offset:128
	ds_read_b128 v[170:173], v224 offset:192
	ds_read_b128 v[178:181], v224 offset:4736
	ds_read_b128 v[150:153], v224 offset:4800
	ds_read_b128 v[130:133], v4 offset:9216
	ds_read_b128 v[134:137], v4 offset:10752
	ds_read_b128 v[138:141], v4 offset:12288
	ds_read_b128 v[142:145], v4 offset:13824
	ds_read_b128 v[146:149], v4 offset:15360
	ds_read_b128 v[126:129], v4 offset:16896
	ds_read_b128 v[122:125], v4 offset:18432
	ds_read_b128 v[118:121], v4 offset:19968
	s_andn2_b64 vcc, exec, s[16:17]
	s_cbranch_vccnz .LBB0_1602
	s_waitcnt lgkmcnt(14)
	v_mfma_f32_16x16x32_bf16 v[182:185], v[154:157], v[22:25], 0
	s_mov_b64 s[16:17], -1
	s_cmp_lt_u32 s28, 23
	s_waitcnt lgkmcnt(13)
	v_mfma_f32_16x16x32_bf16 v[186:189], v[174:177], v[22:25], 0
	v_mfma_f32_16x16x32_bf16 v[182:185], v[158:161], v[26:29], v[182:185]
	s_waitcnt lgkmcnt(12)
	v_mfma_f32_16x16x32_bf16 v[186:189], v[162:165], v[26:29], v[186:189]
	s_waitcnt lgkmcnt(11)
	v_mfma_f32_16x16x32_bf16 v[182:185], v[166:169], v[30:33], v[182:185]
	s_waitcnt lgkmcnt(9)
	v_mfma_f32_16x16x32_bf16 v[186:189], v[178:181], v[30:33], v[186:189]
	v_mfma_f32_16x16x32_bf16 v[182:185], v[170:173], v[34:37], v[182:185]
	s_waitcnt lgkmcnt(8)
	v_mfma_f32_16x16x32_bf16 v[186:189], v[150:153], v[34:37], v[186:189]
	s_cbranch_scc1 .LBB0_1597
	s_nop 4
	v_mul_f32_e32 v210, s8, v182
	v_mul_f32_e32 v211, s8, v183
	v_mul_f32_e32 v212, s8, v184
	v_mul_f32_e32 v213, s8, v185
	v_mul_f32_e32 v4, s8, v186
	v_mul_f32_e32 v5, s8, v187
	v_mul_f32_e32 v208, s8, v188
	v_mul_f32_e32 v209, s8, v189
	s_mov_b64 s[16:17], 0
.LBB0_1597:
	s_andn2_b64 vcc, exec, s[16:17]
	s_cbranch_vccnz .LBB0_1599
	s_sub_i32 s17, s6, s20
	s_max_i32 s17, s17, -7
	s_add_i32 s17, s17, 7
	s_mul_i32 s16, s18, 0x780
	s_min_u32 s17, s17, 14
	s_add_i32 s16, s16, 0
	s_lshl_b32 s17, s17, 7
	s_add_i32 s16, s16, s17
	v_lshl_add_u32 v4, v227, 2, s16
	v_lshl_add_u32 v5, v228, 2, s16
	v_lshl_add_u32 v208, v229, 2, s16
	v_lshl_add_u32 v209, v230, 2, s16
	v_lshl_add_u32 v210, v231, 2, s16
	v_lshl_add_u32 v211, v232, 2, s16
	v_lshl_add_u32 v212, v233, 2, s16
	v_lshl_add_u32 v213, v234, 2, s16
	ds_read_b32 v4, v4 offset:43008
	ds_read_b32 v5, v5 offset:43008
	ds_read_b32 v208, v208 offset:43008
	ds_read_b32 v209, v209 offset:43008
	ds_read_b32 v238, v210 offset:43008
	ds_read_b32 v239, v211 offset:43008
	ds_read_b32 v240, v212 offset:43008
	ds_read_b32 v241, v213 offset:43008
	s_waitcnt lgkmcnt(6)
	v_fma_f32 v210, v182, s8, v4
	v_fma_f32 v211, v183, s8, v5
	s_waitcnt lgkmcnt(4)
	v_fma_f32 v212, v184, s8, v208
	v_fma_f32 v213, v185, s8, v209
	s_waitcnt lgkmcnt(2)
	v_fma_f32 v4, v186, s8, v238
	v_fma_f32 v5, v187, s8, v239
	s_waitcnt lgkmcnt(0)
	v_fma_f32 v208, v188, s8, v240
	v_fma_f32 v209, v189, s8, v241

.LBB0_1602:
	s_or_b64 s[0:1], s[0:1], s[14:15]
	s_andn2_b64 vcc, exec, s[0:1]
	s_cbranch_vccnz .LBB0_1610
	s_waitcnt lgkmcnt(14)
	v_mfma_f32_16x16x32_bf16 v[154:157], v[154:157], v[38:41], 0
	s_mov_b64 s[0:1], -1
	s_cmp_lt_u32 s28, 23
	s_waitcnt lgkmcnt(13)
	v_mfma_f32_16x16x32_bf16 v[174:177], v[174:177], v[38:41], 0
	v_mfma_f32_16x16x32_bf16 v[154:157], v[158:161], v[42:45], v[154:157]
	s_waitcnt lgkmcnt(12)
	v_mfma_f32_16x16x32_bf16 v[158:161], v[162:165], v[42:45], v[174:177]
	s_waitcnt lgkmcnt(11)
	v_mfma_f32_16x16x32_bf16 v[154:157], v[166:169], v[46:49], v[154:157]
	s_waitcnt lgkmcnt(9)
	v_mfma_f32_16x16x32_bf16 v[164:167], v[178:181], v[46:49], v[158:161]
	v_mfma_f32_16x16x32_bf16 v[154:157], v[170:173], v[50:53], v[154:157]
	s_waitcnt lgkmcnt(8)
	v_mfma_f32_16x16x32_bf16 v[150:153], v[150:153], v[50:53], v[164:167]
	s_cbranch_scc1 .LBB0_1605
	s_nop 4
	v_mul_f32_e32 v160, s8, v154
	v_mul_f32_e32 v161, s8, v155
	v_mul_f32_e32 v162, s8, v156
	v_mul_f32_e32 v163, s8, v157
	v_mul_f32_e32 v4, s8, v150
	v_mul_f32_e32 v5, s8, v151
	v_mul_f32_e32 v158, s8, v152
	v_mul_f32_e32 v159, s8, v153
	s_mov_b64 s[0:1], 0
.LBB0_1605:
	s_andn2_b64 vcc, exec, s[0:1]
	s_cbranch_vccnz .LBB0_1607
	s_sub_i32 s1, s6, s21
	s_max_i32 s1, s1, -7
	s_add_i32 s1, s1, 7
	s_mul_i32 s0, s18, 0x780
	s_min_u32 s1, s1, 14
	s_add_i32 s0, s0, 0
	s_lshl_b32 s1, s1, 7
	s_add_i32 s0, s0, s1
	v_lshl_add_u32 v4, v227, 2, s0
	v_lshl_add_u32 v5, v228, 2, s0
	v_lshl_add_u32 v158, v229, 2, s0
	v_lshl_add_u32 v159, v230, 2, s0
	v_lshl_add_u32 v160, v231, 2, s0
	v_lshl_add_u32 v161, v232, 2, s0
	v_lshl_add_u32 v162, v233, 2, s0
	v_lshl_add_u32 v163, v234, 2, s0
	ds_read_b32 v4, v4 offset:43008
	ds_read_b32 v5, v5 offset:43008
	ds_read_b32 v158, v158 offset:43008
	ds_read_b32 v159, v159 offset:43008
	ds_read_b32 v164, v160 offset:43008
	ds_read_b32 v165, v161 offset:43008
	ds_read_b32 v166, v162 offset:43008
	ds_read_b32 v167, v163 offset:43008
	s_waitcnt lgkmcnt(6)
	v_fma_f32 v160, v154, s8, v4
	v_fma_f32 v161, v155, s8, v5
	s_waitcnt lgkmcnt(4)
	v_fma_f32 v162, v156, s8, v158
	v_fma_f32 v163, v157, s8, v159
	s_waitcnt lgkmcnt(2)
	v_fma_f32 v4, v150, s8, v164
	v_fma_f32 v5, v151, s8, v165
	s_waitcnt lgkmcnt(0)
	v_fma_f32 v158, v152, s8, v166
	v_fma_f32 v159, v153, s8, v167

.LBB0_1643:
	s_add_i32 s6, s24, s28
	s_cmp_gt_u32 s28, 22
	s_cselect_b64 s[0:1], -1, 0
	s_cmp_ge_i32 s6, s22
	s_cselect_b64 s[14:15], -1, 0
	s_cmp_lt_i32 s6, s26
	s_cselect_b64 s[16:17], -1, 0
	s_and_b64 s[14:15], s[14:15], s[16:17]
	s_or_b64 s[16:17], s[0:1], s[14:15]
	s_cmp_ge_i32 s6, s23
	s_cselect_b64 s[14:15], -1, 0
	s_cmp_lt_i32 s6, s27
	s_cselect_b64 s[26:27], -1, 0
	s_and_b64 s[14:15], s[14:15], s[26:27]
	s_or_b64 s[26:27], s[16:17], s[14:15]
	s_andn2_b64 vcc, exec, s[26:27]
	s_cbranch_vccnz .LBB0_1660
	v_add_u32_e32 v4, v225, v226
	ds_read_b128 v[154:157], v224 offset:21504
	ds_read_b128 v[158:161], v224 offset:21568
	ds_read_b128 v[174:177], v224 offset:26112
	ds_read_b128 v[162:165], v224 offset:26176
	ds_read_b128 v[166:169], v224 offset:21632
	ds_read_b128 v[170:173], v224 offset:21696
	ds_read_b128 v[178:181], v224 offset:26240
	ds_read_b128 v[150:153], v224 offset:26304
	ds_read_b128 v[130:133], v4 offset:30720
	ds_read_b128 v[134:137], v4 offset:32256
	ds_read_b128 v[138:141], v4 offset:33792
	ds_read_b128 v[142:145], v4 offset:35328
	ds_read_b128 v[146:149], v4 offset:36864
	ds_read_b128 v[126:129], v4 offset:38400
	ds_read_b128 v[122:125], v4 offset:39936
	ds_read_b128 v[118:121], v4 offset:41472
	s_andn2_b64 vcc, exec, s[16:17]
	s_cbranch_vccnz .LBB0_1652
	s_waitcnt lgkmcnt(14)
	v_mfma_f32_16x16x32_bf16 v[182:185], v[154:157], v[22:25], 0
	s_mov_b64 s[16:17], -1
	s_cmp_lt_u32 s28, 23
	s_waitcnt lgkmcnt(13)
	v_mfma_f32_16x16x32_bf16 v[186:189], v[174:177], v[22:25], 0
	v_mfma_f32_16x16x32_bf16 v[182:185], v[158:161], v[26:29], v[182:185]
	s_waitcnt lgkmcnt(12)
	v_mfma_f32_16x16x32_bf16 v[186:189], v[162:165], v[26:29], v[186:189]
	s_waitcnt lgkmcnt(11)
	v_mfma_f32_16x16x32_bf16 v[182:185], v[166:169], v[30:33], v[182:185]
	s_waitcnt lgkmcnt(9)
	v_mfma_f32_16x16x32_bf16 v[186:189], v[178:181], v[30:33], v[186:189]
	v_mfma_f32_16x16x32_bf16 v[182:185], v[170:173], v[34:37], v[182:185]
	s_waitcnt lgkmcnt(8)
	v_mfma_f32_16x16x32_bf16 v[186:189], v[150:153], v[34:37], v[186:189]
	s_cbranch_scc1 .LBB0_1647
	s_nop 4
	v_mul_f32_e32 v4, s8, v182
	v_mul_f32_e32 v5, s8, v183
	v_mul_f32_e32 v210, s8, v184
	v_mul_f32_e32 v211, s8, v185
	v_mul_f32_e32 v208, s8, v186
	v_mul_f32_e32 v209, s8, v187
	v_mul_f32_e32 v212, s8, v188
	v_mul_f32_e32 v213, s8, v189
	s_mov_b64 s[16:17], 0
.LBB0_1647:
	s_andn2_b64 vcc, exec, s[16:17]
	s_cbranch_vccnz .LBB0_1649
	s_sub_i32 s17, s6, s20
	s_max_i32 s17, s17, -7
	s_add_i32 s17, s17, 7
	s_mul_i32 s16, s18, 0x780
	s_min_u32 s17, s17, 14
	s_add_i32 s16, s16, 0
	s_lshl_b32 s17, s17, 7
	s_add_i32 s16, s16, s17
	v_lshl_add_u32 v4, v227, 2, s16
	v_lshl_add_u32 v5, v228, 2, s16
	v_lshl_add_u32 v208, v229, 2, s16
	v_lshl_add_u32 v209, v230, 2, s16
	v_lshl_add_u32 v239, v234, 2, s16
	v_lshl_add_u32 v210, v231, 2, s16
	v_lshl_add_u32 v211, v232, 2, s16
	v_lshl_add_u32 v214, v233, 2, s16
	ds_read_b32 v4, v4 offset:43008
	ds_read_b32 v5, v5 offset:43008
	ds_read_b32 v208, v208 offset:43008
	ds_read_b32 v209, v209 offset:43008
	ds_read_b32 v212, v210 offset:43008
	ds_read_b32 v213, v211 offset:43008
	ds_read_b32 v238, v214 offset:43008
	ds_read_b32 v239, v239 offset:43008
	s_waitcnt lgkmcnt(6)
	v_fma_f32 v4, v182, s8, v4
	v_fma_f32 v5, v183, s8, v5
	s_waitcnt lgkmcnt(4)
	v_fma_f32 v210, v184, s8, v208
	v_fma_f32 v211, v185, s8, v209
	s_waitcnt lgkmcnt(2)
	v_fma_f32 v208, v186, s8, v212
	v_fma_f32 v209, v187, s8, v213
	s_waitcnt lgkmcnt(0)
	v_fma_f32 v212, v188, s8, v238
	v_fma_f32 v213, v189, s8, v239

.LBB0_1652:
	s_or_b64 s[0:1], s[0:1], s[14:15]
	s_andn2_b64 vcc, exec, s[0:1]
	s_cbranch_vccnz .LBB0_1660
	s_waitcnt lgkmcnt(14)
	v_mfma_f32_16x16x32_bf16 v[154:157], v[154:157], v[38:41], 0
	s_mov_b64 s[0:1], -1
	s_cmp_lt_u32 s28, 23
	s_waitcnt lgkmcnt(13)
	v_mfma_f32_16x16x32_bf16 v[174:177], v[174:177], v[38:41], 0
	v_mfma_f32_16x16x32_bf16 v[154:157], v[158:161], v[42:45], v[154:157]
	s_waitcnt lgkmcnt(12)
	v_mfma_f32_16x16x32_bf16 v[158:161], v[162:165], v[42:45], v[174:177]
	s_waitcnt lgkmcnt(11)
	v_mfma_f32_16x16x32_bf16 v[154:157], v[166:169], v[46:49], v[154:157]
	s_waitcnt lgkmcnt(9)
	v_mfma_f32_16x16x32_bf16 v[164:167], v[178:181], v[46:49], v[158:161]
	v_mfma_f32_16x16x32_bf16 v[154:157], v[170:173], v[50:53], v[154:157]
	s_waitcnt lgkmcnt(8)
	v_mfma_f32_16x16x32_bf16 v[150:153], v[150:153], v[50:53], v[164:167]
	s_cbranch_scc1 .LBB0_1655
	s_nop 4
	v_mul_f32_e32 v4, s8, v154
	v_mul_f32_e32 v5, s8, v155
	v_mul_f32_e32 v160, s8, v156
	v_mul_f32_e32 v161, s8, v157
	v_mul_f32_e32 v158, s8, v150
	v_mul_f32_e32 v159, s8, v151
	v_mul_f32_e32 v162, s8, v152
	v_mul_f32_e32 v163, s8, v153
	s_mov_b64 s[0:1], 0
.LBB0_1655:
	s_andn2_b64 vcc, exec, s[0:1]
	s_cbranch_vccnz .LBB0_1657
	s_sub_i32 s1, s6, s21
	s_max_i32 s1, s1, -7
	s_add_i32 s1, s1, 7
	s_mul_i32 s0, s18, 0x780
	s_min_u32 s1, s1, 14
	s_add_i32 s0, s0, 0
	s_lshl_b32 s1, s1, 7
	s_add_i32 s0, s0, s1
	v_lshl_add_u32 v4, v227, 2, s0
	v_lshl_add_u32 v5, v228, 2, s0
	v_lshl_add_u32 v158, v229, 2, s0
	v_lshl_add_u32 v159, v230, 2, s0
	v_lshl_add_u32 v164, v233, 2, s0
	v_lshl_add_u32 v165, v234, 2, s0
	v_lshl_add_u32 v160, v231, 2, s0
	v_lshl_add_u32 v161, v232, 2, s0
	ds_read_b32 v4, v4 offset:43008
	ds_read_b32 v5, v5 offset:43008
	ds_read_b32 v158, v158 offset:43008
	ds_read_b32 v159, v159 offset:43008
	ds_read_b32 v162, v160 offset:43008
	ds_read_b32 v163, v161 offset:43008
	ds_read_b32 v164, v164 offset:43008
	ds_read_b32 v165, v165 offset:43008
	s_waitcnt lgkmcnt(6)
	v_fma_f32 v4, v154, s8, v4
	v_fma_f32 v5, v155, s8, v5
	s_waitcnt lgkmcnt(4)
	v_fma_f32 v160, v156, s8, v158
	v_fma_f32 v161, v157, s8, v159
	s_waitcnt lgkmcnt(2)
	v_fma_f32 v158, v150, s8, v162
	v_fma_f32 v159, v151, s8, v163
	s_waitcnt lgkmcnt(0)
	v_fma_f32 v162, v152, s8, v164
	v_fma_f32 v163, v153, s8, v165
